# attention loop: next unit's decode and loads issued before the current unit's staging (K/V rows copied to unused registers first)
# baseline (speedup 1.0000x reference)
.LBB0_353:
	s_lshl_b32 s30, 1, s16
	s_add_u32 s33, s92, 0xa1400000
	s_addc_u32 s78, s93, 0
	s_add_u32 s34, s92, 0x57400000
	s_addc_u32 s35, s93, 0
	s_add_u32 s40, s92, 0x600000
	v_mov_b32_e32 v11, 0
	v_add_lshl_u32 v10, s14, v107, 7
	s_addc_u32 s41, s93, 0
	s_lshl_b32 s16, s22, 4
	v_lshl_add_u64 v[96:97], s[10:11], 0, v[6:7]
	v_lshl_add_u64 v[98:99], s[12:13], 0, v[6:7]
	v_lshl_add_u64 v[6:7], v[4:5], 0, v[10:11]
	v_lshl_add_u64 v[8:9], v[2:3], 0, v[10:11]
	global_load_dwordx4 v[30:33], v[6:7], off
	global_load_dwordx4 v[34:37], v[8:9], off
	v_or_b32_e32 v6, s14, v105
	s_add_u32 s8, s33, s8
	v_and_b32_e32 v46, 15, v0
	v_lshlrev_b32_e32 v10, 7, v6
	s_addc_u32 s9, s78, s9
	s_add_i32 s10, s14, s16
	v_lshl_add_u64 v[4:5], v[4:5], 0, v[10:11]
	v_lshl_add_u64 v[2:3], v[2:3], 0, v[10:11]
	v_or_b32_e32 v10, s10, v46
	v_lshlrev_b32_e32 v47, 1, v0
	global_load_dwordx4 v[38:41], v[4:5], off
	global_load_dwordx4 v[42:45], v[2:3], off
	v_lshlrev_b64 v[2:3], 7, v[10:11]
	v_and_b32_e32 v94, 0x60, v47
	v_mov_b32_e32 v95, v11
	v_lshl_add_u64 v[2:3], s[8:9], 0, v[2:3]
	v_lshl_add_u64 v[2:3], v[2:3], 0, v[94:95]
	global_load_dwordx4 v[6:9], v[2:3], off offset:16
	s_nop 0
	global_load_dwordx4 v[2:5], v[2:3], off
	v_and_b32_e32 v10, 7, v0
	v_or_b32_e32 v108, s16, v46
	v_lshlrev_b32_e32 v46, 1, v10
	v_lshlrev_b32_e32 v10, 4, v10
	v_and_b32_e32 v52, 0x50, v0
	v_xad_u32 v10, v10, v52, 0
	v_lshrrev_b32_e32 v52, 1, v0
	v_bfe_u32 v50, v0, 5, 2
	v_or_b32_e32 v51, 1, v46
	v_and_b32_e32 v53, 4, v52
	v_and_b32_e32 v52, 12, v52
	v_lshlrev_b32_e32 v61, 2, v107
	v_bitop3_b32 v60, v52, v46, v50 bitop3:0x36
	v_bitop3_b32 v52, v52, v51, v50 bitop3:0x36
	s_add_i32 s21, 0, 0x10000
	v_and_b32_e32 v61, 12, v61
	v_lshlrev_b32_e32 v59, 8, v105
	v_lshl_add_u32 v60, v60, 4, s21
	v_lshl_add_u32 v52, v52, 4, s21
	v_bitop3_b32 v62, v61, v46, v50 bitop3:0x36
	v_bitop3_b32 v61, v61, v51, v50 bitop3:0x36
	v_add_u32_e32 v115, v60, v59
	v_add_u32_e32 v116, v52, v59
	v_lshlrev_b32_e32 v59, 8, v107
	v_lshlrev_b32_e32 v62, 4, v62
	v_lshlrev_b32_e32 v61, 4, v61
	v_add3_u32 v118, s21, v62, v59
	v_add3_u32 v119, s21, v61, v59
	v_or_b32_e32 v59, 0x80, v105
	v_lshlrev_b32_e32 v61, 8, v59
	v_add_u32_e32 v122, v52, v61
	v_add_u32_e32 v52, 0x80, v107
	s_movk_i32 s14, 0x1e0
	v_and_b32_e32 v48, 3, v0
	s_and_b32 s17, s22, 0x3fffffe
	v_and_or_b32 v47, v47, 8, v53
	v_lshrrev_b32_e32 v53, 1, v1
	v_and_b32_e32 v54, 4, v105
	v_lshl_add_u32 v114, v105, 7, v10
	v_lshl_add_u32 v117, v107, 7, v10
	v_lshl_add_u32 v120, v59, 7, v10
	v_lshl_add_u32 v123, v52, 7, v10
	v_add3_u32 v10, v0, v13, s14
	s_movk_i32 s14, 0x81
	v_and_or_b32 v53, v53, 8, v54
	v_lshrrev_b32_e32 v54, 3, v1
	s_add_i32 s18, 0, 0x20000
	s_lshl_b32 s19, s17, 4
	v_cmp_gt_u32_e64 s[14:15], s14, v10
	v_or_b32_e32 v10, v47, v48
	v_and_b32_e32 v54, 6, v54
	v_lshl_add_u32 v127, v12, 2, s18
	v_or_b32_e32 v12, s19, v10
	s_sub_i32 s79, 8, s17
	v_or_b32_e32 v55, 1, v54
	v_mov_b32_e32 v57, s18
	s_add_i32 s20, s19, 32
	v_lshl_add_u32 v126, v0, 2, s18
	v_readlane_b32 s18, v254, 8
	v_lshlrev_b32_e32 v128, 7, v12
	v_lshrrev_b32_e32 v12, 1, v10
	s_cmpk_lt_u32 s18, 0x200
	v_bitop3_b32 v13, v12, v54, 5 bitop3:0x6c
	v_bitop3_b32 v12, v12, v55, 5 bitop3:0x6c
	s_cselect_b64 s[46:47], -1, 0
	v_lshlrev_b32_e32 v129, 4, v13
	v_lshlrev_b32_e32 v130, 4, v12
	v_or3_b32 v12, v48, s16, v47
	v_mov_b32_e32 v13, 0x800
	s_cmpk_lt_u32 s18, 0x180
	v_lshl_or_b32 v131, v12, 7, v13
	v_lshrrev_b32_e32 v12, 1, v12
	s_cselect_b64 s[48:49], -1, 0
	s_cmp_lt_u32 s17, 5
	v_bitop3_b32 v13, v12, v54, 5 bitop3:0x6c
	v_bitop3_b32 v12, v12, v55, 5 bitop3:0x6c
	s_cselect_b64 s[50:51], -1, 0
	s_add_i32 s16, s19, 48
	v_lshlrev_b32_e32 v133, 4, v12
	v_or_b32_e32 v12, s20, v10
	s_cmpk_lt_u32 s18, 0x100
	v_lshlrev_b32_e32 v134, 7, v12
	v_or_b32_e32 v12, s16, v10
	s_cselect_b64 s[52:53], -1, 0
	s_add_i32 s16, s19, 64
	s_cmp_lt_u32 s17, 3
	v_sub_u32_e32 v56, 0, v0
	v_lshlrev_b32_e32 v135, 7, v12
	v_or_b32_e32 v12, s16, v10
	s_cselect_b64 s[54:55], -1, 0
	s_add_i32 s16, s19, 0x50
	v_and_b32_e32 v56, 3, v56
	s_movk_i32 s10, 0x350
	s_cmpk_lt_u32 s18, 0x80
	v_mad_u32_u24 v57, v56, s10, v57
	v_add_u32_e32 v56, v108, v56
	v_lshlrev_b32_e32 v136, 7, v12
	v_or_b32_e32 v12, s16, v10
	s_cselect_b64 s[56:57], -1, 0
	s_add_i32 s16, s19, 0x60
	v_sub_u32_e32 v56, s19, v56
	v_lshlrev_b32_e32 v137, 7, v12
	v_or_b32_e32 v12, s16, v10
	s_add_i32 s16, s19, 0x70
	v_bfe_u32 v49, v0, 2, 2
	v_lshlrev_b32_e32 v56, 2, v56
	v_lshlrev_b32_e32 v58, 2, v53
	v_lshlrev_b32_e32 v138, 7, v12
	v_or_b32_e32 v12, s16, v10
	s_add_i32 s16, s19, 0x80
	v_add3_u32 v111, v57, v56, v58
	v_add_u32_e32 v113, 0x290, v57
	v_or3_b32 v49, v53, s19, v49
	v_bfe_u32 v56, v0, 1, 1
	v_and_b32_e32 v57, 12, v0
	v_lshrrev_b32_e32 v53, 2, v53
	v_lshlrev_b32_e32 v139, 7, v12
	v_or_b32_e32 v12, s16, v10
	v_lshlrev_b32_e32 v140, 7, v12
	v_bitop3_b32 v12, v53, v56, v57 bitop3:0x36
	v_lshlrev_b32_e32 v149, 4, v12
	v_or_b32_e32 v12, 2, v56
	v_bitop3_b32 v12, v53, v12, v57 bitop3:0x36
	v_lshlrev_b32_e32 v150, 4, v12
	v_or_b32_e32 v12, 4, v56
	v_bitop3_b32 v12, v53, v12, v57 bitop3:0x36
	v_lshlrev_b32_e32 v151, 4, v12
	v_or_b32_e32 v12, 6, v56
	v_bitop3_b32 v12, v53, v12, v57 bitop3:0x36
	v_lshlrev_b32_e32 v152, 4, v12
	v_or_b32_e32 v12, 8, v56
	v_bitop3_b32 v12, v53, v12, v57 bitop3:0x36
	v_lshlrev_b32_e32 v153, 4, v12
	v_or_b32_e32 v12, 10, v56
	v_bitop3_b32 v12, v53, v12, v57 bitop3:0x36
	v_add_u32_e32 v121, v60, v61
	v_lshlrev_b32_e32 v60, 2, v52
	s_addk_i32 s19, 0x90
	v_lshlrev_b32_e32 v154, 4, v12
	v_or_b32_e32 v12, 12, v56
	v_lshlrev_b32_e32 v58, 3, v0
	v_and_b32_e32 v60, 12, v60
	v_or_b32_e32 v10, s19, v10
	v_bitop3_b32 v12, v53, v12, v57 bitop3:0x36
	v_and_b32_e32 v58, 8, v58
	v_bitop3_b32 v46, v60, v46, v50 bitop3:0x36
	v_bitop3_b32 v50, v60, v51, v50 bitop3:0x36
	v_lshlrev_b32_e32 v141, 7, v10
	v_lshlrev_b32_e32 v10, 8, v49
	v_lshlrev_b32_e32 v155, 4, v12
	v_or_b32_e32 v12, 14, v56
	v_lshlrev_b32_e32 v59, 8, v52
	v_lshlrev_b32_e32 v46, 4, v46
	v_lshlrev_b32_e32 v50, 4, v50
	s_movk_i32 s12, 0x150
	v_bitop3_b32 v12, v53, v12, v57 bitop3:0x36
	v_add3_u32 v157, s21, v10, v58
	v_mbcnt_lo_u32_b32 v10, -1, 0
	v_or_b32_e32 v110, 0xffffff80, v105
	v_add_u32_e32 v112, 0x80, v111
	v_cmp_gt_u32_e64 s[8:9], 16, v1
	v_add3_u32 v124, s21, v46, v59
	v_add3_u32 v125, s21, v50, v59
	v_cmp_gt_u32_e64 s[10:11], s10, v0
	v_cmp_gt_u32_e64 s[12:13], s12, v0
	v_lshlrev_b32_e32 v132, 4, v13
	v_add_u32_e32 v142, 0xc0, v111
	v_add_u32_e32 v143, 0x100, v111
	v_add_u32_e32 v144, 0x140, v111
	v_add_u32_e32 v145, 0x180, v111
	v_add_u32_e32 v146, 0x1c0, v111
	v_add_u32_e32 v147, 0x200, v111
	v_add_u32_e32 v148, 0x240, v111
	v_lshlrev_b32_e32 v156, 4, v12
	v_and_b32_e32 v100, 48, v0
	v_mov_b32_e32 v101, v11
	s_mov_b32 s80, 0x800000
	s_mov_b32 s94, 0x3f317217
	s_mov_b32 s76, 0x7f800000
	s_mov_b32 s77, 0x409b43d5
	s_mov_b32 s36, s31
	s_mov_b32 s37, s31
	s_mov_b32 s38, s31
	s_mov_b32 s39, s31
	v_mbcnt_hi_u32_b32 v158, -1, v10
	v_mov_b32_e32 v159, 0xff800000
	v_mov_b32_e32 v160, 0x41b17218
	s_mov_b32 s81, 0
	s_waitcnt vmcnt(0)
	s_branch .LBB0_355

.LBB0_355:
	s_lshl_b32 s43, s81, 15
	s_lshl_b32 s87, s81, 14
	s_mov_b64 s[100:101], s[44:45]
	s_waitcnt vmcnt(3)
	v_mov_b64_e32 v[212:213], v[14:15]
	v_mov_b64_e32 v[214:215], v[16:17]
	v_mov_b64_e32 v[216:217], v[18:19]
	v_mov_b64_e32 v[218:219], v[20:21]
	v_mov_b64_e32 v[220:221], v[22:23]
	v_mov_b64_e32 v[222:223], v[24:25]
	v_mov_b64_e32 v[224:225], v[26:27]
	v_mov_b64_e32 v[226:227], v[28:29]
	v_mov_b64_e32 v[228:229], v[30:31]
	v_mov_b64_e32 v[230:231], v[32:33]
	v_mov_b64_e32 v[232:233], v[34:35]
	v_mov_b64_e32 v[234:235], v[36:37]
	v_mov_b64_e32 v[236:237], v[38:39]
	v_mov_b64_e32 v[238:239], v[40:41]
	v_mov_b64_e32 v[240:241], v[42:43]
	v_mov_b64_e32 v[242:243], v[44:45]
	v_mov_b32_e32 v244, v104
	v_mov_b32_e32 v245, v109
	s_add_i32 s3, s3, 1
	s_cmp_ge_i32 s3, s2
	s_cselect_b64 s[58:59], -1, 0
	s_and_b64 vcc, exec, s[58:59]
	s_cbranch_vccnz .LBB0_369
	s_mul_hi_i32 s16, s3, 0x2aaaaaab
	s_lshr_b32 s17, s16, 31
	s_lshr_b32 s16, s16, 9
	s_add_i32 s16, s16, s17
	s_mulk_i32 s16, 0xc00
	s_sub_i32 s20, s3, s16
	s_mul_i32 s16, s20, 0x2aab
	s_lshr_b32 s17, s16, 31
	s_ashr_i32 s21, s16, 17
	s_add_i32 s21, s21, s17
	s_mul_i32 s16, s21, -12
	s_add_i32 s16, s16, s20
	s_ashr_i32 s82, s16, 2
	s_lshl_b32 s22, s82, 1
	v_lshlrev_b32_e32 v10, s22, v102
	v_cmp_lt_i32_e32 vcc, 15, v10
	s_and_saveexec_b64 s[16:17], vcc
	s_cbranch_execz .LBB0_364
	v_cvt_f32_u32_e32 v10, v10
	v_mul_f32_e32 v10, 0x3d800000, v10
	v_cmp_gt_f32_e32 vcc, s80, v10
	s_nop 1
	v_cndmask_b32_e64 v12, 0, 32, vcc
	v_ldexp_f32 v10, v10, v12
	v_log_f32_e32 v10, v10
	v_cndmask_b32_e32 v12, 0, v160, vcc
	v_mul_f32_e32 v13, 0x3f317217, v10
	v_fma_f32 v13, v10, s94, -v13
	v_fmac_f32_e32 v13, 0x3377d1cf, v10
	v_fmac_f32_e32 v13, 0x3f317217, v10
	v_cmp_lt_f32_e64 vcc, |v10|, s76
	s_nop 1
	v_cndmask_b32_e32 v10, v10, v13, vcc
	v_sub_f32_e32 v10, v10, v12
	v_div_scale_f32 v12, s[18:19], s77, s77, v10
	v_rcp_f32_e32 v13, v12
	v_div_scale_f32 v14, vcc, v10, s77, v10
	v_fma_f32 v15, -v12, v13, 1.0
	v_fmac_f32_e32 v13, v15, v13
	v_mul_f32_e32 v15, v14, v13
	v_fma_f32 v16, -v12, v15, v14
	v_fmac_f32_e32 v15, v16, v13
	v_fma_f32 v12, -v12, v15, v14
	v_div_fmas_f32 v12, v12, v13, v15
	v_div_fixup_f32 v10, v12, s77, v10
	v_mul_f32_e32 v10, 0x41800000, v10
	v_cvt_i32_f32_e32 v10, v10
	v_min_i32_e32 v10, 15, v10
	v_add_u32_e32 v10, 16, v10

.Lat_stage:
	s_andn2_b64 vcc, exec, s[100:101]
	s_cbranch_vccnz .LBB0_357
	v_add_u32_e32 v10, s87, v114
	v_cvt_pk_f32_fp8_sdwa v[248:249], v216 src0_sel:WORD_1
	v_cvt_pk_f32_fp8_sdwa v[252:253], v217 src0_sel:WORD_1
	ds_write_b128 v10, v[212:215]
	v_cvt_pk_f32_fp8_e32 v[12:13], v216
	v_cvt_pk_f32_fp8_e32 v[250:251], v217
	v_cvt_pk_bf16_f32 v246, v12, v13
	v_cvt_pk_bf16_f32 v247, v248, v249
	v_cvt_pk_bf16_f32 v248, v250, v251
	v_cvt_pk_bf16_f32 v249, v252, v253
	v_cvt_pk_f32_fp8_sdwa v[252:253], v218 src0_sel:WORD_1
	v_add_u32_e32 v10, s43, v115
	v_cvt_pk_f32_fp8_e32 v[12:13], v218
	v_cvt_pk_f32_fp8_e32 v[54:55], v219
	v_cvt_pk_f32_fp8_sdwa v[56:57], v219 src0_sel:WORD_1
	v_cvt_pk_bf16_f32 v250, v12, v13
	v_cvt_pk_bf16_f32 v251, v252, v253
	v_cvt_pk_bf16_f32 v252, v54, v55
	v_cvt_pk_bf16_f32 v253, v56, v57
	v_add_u32_e32 v58, s43, v116
	ds_write_b128 v10, v[246:249]
	ds_write_b128 v58, v[250:253]
	v_add_u32_e32 v10, s87, v117
	v_cvt_pk_f32_fp8_sdwa v[248:249], v224 src0_sel:WORD_1
	v_cvt_pk_f32_fp8_sdwa v[252:253], v225 src0_sel:WORD_1
	ds_write_b128 v10, v[220:223]
	v_cvt_pk_f32_fp8_e32 v[12:13], v224
	v_add_u32_e32 v10, s43, v118
	v_cvt_pk_f32_fp8_e32 v[250:251], v225
	v_cvt_pk_bf16_f32 v246, v12, v13
	v_cvt_pk_bf16_f32 v247, v248, v249
	v_cvt_pk_bf16_f32 v248, v250, v251
	v_cvt_pk_bf16_f32 v249, v252, v253
	v_cvt_pk_f32_fp8_sdwa v[252:253], v226 src0_sel:WORD_1
	v_add_u32_e32 v58, s43, v119
	v_cvt_pk_f32_fp8_e32 v[12:13], v226
	v_cvt_pk_f32_fp8_e32 v[54:55], v227
	v_cvt_pk_f32_fp8_sdwa v[56:57], v227 src0_sel:WORD_1
	v_cvt_pk_bf16_f32 v250, v12, v13
	v_cvt_pk_bf16_f32 v251, v252, v253
	v_cvt_pk_bf16_f32 v252, v54, v55
	v_cvt_pk_bf16_f32 v253, v56, v57
	ds_write_b128 v10, v[246:249]
	ds_write_b128 v58, v[250:253]
.LBB0_357:
	v_subrev_u32_e32 v10, s87, v120
	v_cvt_pk_f32_fp8_sdwa v[248:249], v236 src0_sel:WORD_1
	v_cvt_pk_f32_fp8_sdwa v[252:253], v237 src0_sel:WORD_1
	ds_write_b128 v10, v[240:243]
	v_cvt_pk_f32_fp8_e32 v[12:13], v236
	v_cvt_pk_f32_fp8_e32 v[250:251], v237
	v_cvt_pk_bf16_f32 v246, v12, v13
	v_cvt_pk_bf16_f32 v247, v248, v249
	v_cvt_pk_bf16_f32 v248, v250, v251
	v_cvt_pk_bf16_f32 v249, v252, v253
	v_cvt_pk_f32_fp8_sdwa v[252:253], v238 src0_sel:WORD_1
	v_subrev_u32_e32 v10, s43, v121
	v_cvt_pk_f32_fp8_e32 v[12:13], v238
	v_cvt_pk_f32_fp8_e32 v[54:55], v239
	v_cvt_pk_f32_fp8_sdwa v[56:57], v239 src0_sel:WORD_1
	v_cvt_pk_bf16_f32 v250, v12, v13
	v_cvt_pk_bf16_f32 v251, v252, v253
	v_cvt_pk_bf16_f32 v252, v54, v55
	v_cvt_pk_bf16_f32 v253, v56, v57
	v_subrev_u32_e32 v58, s43, v122
	ds_write_b128 v10, v[246:249]
	ds_write_b128 v58, v[250:253]
	v_subrev_u32_e32 v10, s87, v123
	v_cvt_pk_f32_fp8_sdwa v[248:249], v228 src0_sel:WORD_1
	v_cvt_pk_f32_fp8_sdwa v[252:253], v229 src0_sel:WORD_1
	ds_write_b128 v10, v[232:235]
	v_cvt_pk_f32_fp8_e32 v[12:13], v228
	v_subrev_u32_e32 v10, s43, v124
	v_cvt_pk_f32_fp8_e32 v[250:251], v229
	v_cvt_pk_bf16_f32 v246, v12, v13
	v_cvt_pk_bf16_f32 v247, v248, v249
	v_cvt_pk_bf16_f32 v248, v250, v251
	v_cvt_pk_bf16_f32 v249, v252, v253
	v_cvt_pk_f32_fp8_sdwa v[252:253], v230 src0_sel:WORD_1
	v_subrev_u32_e32 v58, s43, v125
	v_cvt_pk_f32_fp8_e32 v[12:13], v230
	v_cvt_pk_f32_fp8_e32 v[54:55], v231
	v_cvt_pk_f32_fp8_sdwa v[56:57], v231 src0_sel:WORD_1
	v_cvt_pk_bf16_f32 v250, v12, v13
	v_cvt_pk_bf16_f32 v251, v252, v253
	v_cvt_pk_bf16_f32 v252, v54, v55
	v_cvt_pk_bf16_f32 v253, v56, v57
	ds_write_b128 v10, v[246:249]
	ds_write_b128 v58, v[250:253]
	s_and_saveexec_b64 s[16:17], s[10:11]
	v_mul_f32_e32 v10, 0x3fb8aa3b, v244
	v_cndmask_b32_e64 v10, v159, v10, s[6:7]
	ds_write_b32 v126, v10
	s_or_b64 exec, exec, s[16:17]
	s_and_saveexec_b64 s[16:17], s[12:13]
	v_mul_f32_e32 v10, 0x3fb8aa3b, v245
	v_cndmask_b32_e64 v10, v159, v10, s[14:15]
	ds_write_b32 v127, v10
	s_or_b64 exec, exec, s[16:17]
	s_waitcnt lgkmcnt(0)
	s_barrier
